# rwkv state scan: full-rate 24-bit multiplies also in the peeled last chunk (7 more v_mul_lo_u32 replaced)
# speedup vs baseline: 1.0069x; 1.0069x over previous
; #define LAS __attribute__((address_space(3)))
; __device__ __forceinline__ void rwkv_state_phase(LAS unsigned char* lds, const unsigned char* img, bf16_t* y_, const RwScan& a_, const int vcu, const int G, const int tid0_) {
;     ...
;             if (wave < 4) {
;                 { const int o_ = (tid >> 3) * 144 + (tid & 7) * 16; *(LAS u32x4*)(lb + SK_AT + o_) = q0a; *(LAS u32x4*)(lb + SK_RT + o_) = q0b; }
;                 { const int idx = tid & 127, o_ = (tid >> 7) * 2560 + (idx >> 2) * 80 + (idx & 3) * 16; *(LAS u32x4*)(lb + SK_NAK + o_) = q1a; *(LAS u32x4*)(lb + SK_MKR + o_) = q1b; }
;                 { const int o_ = (tid >> 2) * 80 + (tid & 3) * 16; *(LAS u32x4*)(lb + SK_BH + o_) = q2a; *(LAS u32x4*)(lb + SK_KH + o_) = q2b; }
;                 if (tid < 128) { const int t_ = tid >> 2, i0_ = 8 * (tid & 3); const unsigned wv_[4] = {q3.x, q3.y, q3.z, q3.w};
; #pragma unroll
;                     for (int e = 0; e < 4; ++e) { Vi[(i0_ + 2 * e) * P32 + t_] = (bf16_t)(wv_[e] & 0xffffu); Vi[(i0_ + 2 * e + 1) * P32 + t_] = (bf16_t)(wv_[e] >> 16); } }
;                 else if (tid < 144) *(LAS u32x4*)(lb + SK_PL + (tid - 128) * 16) = q3;
.LBB0_806:
	v_mov_b32_e32 v2, v1
	s_and_b64 vcc, exec, s[8:9]
	s_cbranch_vccnz .LBB0_814
	v_lshrrev_b32_e32 v4, 3, v2
	v_mul_u32_u24_e32 v5, s67, v4
	v_lshlrev_b32_e32 v4, 4, v2
	v_and_b32_e32 v79, 0x70, v4
	v_add3_u32 v5, v5, v79, 0
	s_waitcnt vmcnt(5)
	ds_write_b128 v5, v[42:45] offset:42240
	s_waitcnt vmcnt(4)
	ds_write_b128 v5, v[46:49] offset:46848
	v_lshrrev_b32_e32 v5, 7, v2
	s_movk_i32 s28, 0xa00
	v_mul_u32_u24_e32 v5, s28, v5
	v_bfe_u32 v42, v2, 2, 5
	v_mul_u32_u24_e32 v42, 0x50, v42
	v_and_or_b32 v5, v4, 48, v5
	v_add3_u32 v5, v5, v42, 0
	s_waitcnt vmcnt(3)
	ds_write_b128 v5, v[50:53] offset:56064
	s_waitcnt vmcnt(2)
	ds_write_b128 v5, v[54:57] offset:61184
	v_ashrrev_i32_e32 v5, 2, v2
	v_and_b32_e32 v42, 3, v2
	v_mul_u32_u24_e32 v43, s66, v5
	v_lshlrev_b32_e32 v44, 4, v42
	v_add3_u32 v43, v43, v44, 0
	s_movk_i32 s28, 0x7f
	v_add_u32_e32 v44, 0x12100, v43
	v_add_u32_e32 v43, 0x13500, v43
	v_cmp_lt_i32_e32 vcc, s28, v2
	s_waitcnt vmcnt(1)
	ds_write_b128 v44, v[58:61]
	s_waitcnt vmcnt(0)
	ds_write_b128 v43, v[66:69]
	s_and_saveexec_b64 s[28:29], vcc
	s_xor_b64 s[28:29], exec, s[28:29]
	s_cbranch_execz .LBB0_811
	v_cmp_gt_u32_e32 vcc, s67, v2
	s_and_saveexec_b64 s[34:35], vcc
	s_cbranch_execz .LBB0_810
	v_readlane_b32 s33, v253, 57
	s_nop 1
	v_add_u32_e32 v4, s33, v4
	v_add_u32_e32 v4, 0xfffff800, v4
	ds_write_b128 v4, v[38:41]

; #define LAS __attribute__((address_space(3)))
; __device__ __forceinline__ unsigned cvt_pk_bf16(float lo, float hi) { const f32x2 v = {lo, hi}; const bf16x2_t b = __builtin_convertvector(v, bf16x2_t); return __builtin_bit_cast(unsigned, b); }
; #define ZERO4() ((f32x4){opaque0(), 0.f, 0.f, 0.f} * 0.f)
; __device__ __forceinline__ void rwkv_state_phase(LAS unsigned char* lds, const unsigned char* img, bf16_t* y_, const RwScan& a_, const int vcu, const int G, const int tid0_) {
;     ...
;             { const int mt = wave >> 1, nt = wave & 1; u32x2 o; o.x = cvt_pk_bf16(Sacc[0], Sacc[1]); o.y = cvt_pk_bf16(Sacc[2], Sacc[3]);
;               *(LAS u32x2*)(S0 + (16 * nt + fr) * P64 + 16 * mt + 4 * fq) = o; }
;             __syncthreads();
;             if (ch + 1 < SEQ / 32) ST_FETCH(ch + 1);
;             if (wave >= 4) {
;                 const int mt = (wave - 4) >> 1, nt = (wave - 4) & 1;
;                 f32x4 w = ZERO4();
; #pragma unroll
;                 for (int ks = 0; ks < 2; ++ks) w = __builtin_amdgcn_mfma_f32_16x16x32_bf16(ldfrag(AT, P64, 16 * mt + fr, 32 * ks + 8 * fq), ldfrag(S0, P64, 16 * nt + fr, 32 * ks + 8 * fq), w, 0, 0, 0);
;                 w = __builtin_amdgcn_mfma_f32_16x16x32_bf16(ldfrag(NakT, P32, 16 * mt + fr, 8 * fq), ldfrag(Vi, P32, 16 * nt + fr, 8 * fq), w, 0, 0, 0);
;                 u32x2 o; o.x = cvt_pk_bf16(w[0], w[1]); o.y = cvt_pk_bf16(w[2], w[3]); *(LAS u32x2*)(Wi + (16 * nt + fr) * P32 + 16 * mt + 4 * fq) = o;
;             }
;             __syncthreads();
;             if (wave < 4) {
;                 const int mt = wave >> 1, nt = wave & 1;
;                 f32x4 uu = ZERO4();
;                 uu = __builtin_amdgcn_mfma_f32_16x16x32_bf16(ldfrag(TT, P32, 16 * mt + fr, 8 * fq), ldfrag(Wi, P32, 16 * nt + fr, 8 * fq), uu, 0, 0, 0);
;                 u32x2 o; o.x = cvt_pk_bf16(uu[0], uu[1]); o.y = cvt_pk_bf16(uu[2], uu[3]); *(LAS u32x2*)(Ui + (16 * nt + fr) * P32 + 16 * mt + 4 * fq) = o;
;             }
.LBB0_814:
	s_waitcnt vmcnt(0)
	v_and_b32_e32 v39, 15, v2
	v_bfe_u32 v2, v2, 4, 2
	v_or_b32_e32 v40, s54, v39
	v_mul_u32_u24_e32 v42, 0x90, v40
	v_lshlrev_b32_e32 v41, 3, v2
	v_cvt_pk_bf16_f32 v4, v62, v63
	v_cvt_pk_bf16_f32 v5, v64, v65
	v_add3_u32 v41, s57, v42, v41
	v_lshlrev_b32_e32 v38, 2, v2
	ds_write_b64 v41, v[4:5] offset:51456
	v_lshlrev_b32_e32 v41, 4, v2
	s_and_b64 vcc, exec, s[10:11]
	v_mul_u32_u24_e32 v44, 0x50, v40
	v_lshlrev_b32_e32 v38, 1, v38
	v_add3_u32 v42, 0, v42, v41
	s_waitcnt lgkmcnt(0)
	s_barrier
	s_cbranch_vccnz .LBB0_816
	v_or_b32_e32 v43, s55, v39
	v_mul_u32_u24_e32 v45, s67, v43
	v_mov_b32_e32 v2, v3
	v_add3_u32 v45, 0, v45, v41
	ds_read_b128 v[46:49], v45 offset:42240
	ds_read_b128 v[50:53], v42 offset:51456
	v_mul_f32_e32 v2, 0, v2
	v_mov_b32_e32 v4, v3
	v_mov_b32_e32 v5, v3
	v_readlane_b32 s28, v253, 58
	s_waitcnt lgkmcnt(0)
	v_mfma_f32_16x16x32_bf16 v[46:49], v[46:49], v[50:53], v[2:5]
	ds_read_b128 v[50:53], v45 offset:42304
	ds_read_b128 v[54:57], v42 offset:51520
	s_nop 0
	v_lshlrev_b32_e32 v2, 6, v43
	v_sub_u32_e32 v2, v45, v2
	s_waitcnt lgkmcnt(0)
	v_mfma_f32_16x16x32_bf16 v[46:49], v[50:53], v[54:57], v[46:49]
	ds_read_b128 v[50:53], v2 offset:56064
	v_add3_u32 v2, s28, v44, v41
	ds_read_b128 v[54:57], v2
	v_add3_u32 v2, s56, v44, v38
	s_waitcnt lgkmcnt(0)
	v_mfma_f32_16x16x32_bf16 v[46:49], v[50:53], v[54:57], v[46:49]
	s_nop 7
	v_cvt_pk_bf16_f32 v4, v46, v47
	v_cvt_pk_bf16_f32 v5, v48, v49
	ds_write_b64 v2, v[4:5] offset:26560
.LBB0_816:
	s_and_b64 vcc, exec, s[8:9]
	v_or_b32_e32 v43, s18, v39
	s_waitcnt lgkmcnt(0)
	s_barrier
	s_cbranch_vccnz .LBB0_818
	v_mul_u32_u24_e32 v4, s66, v43
	v_mov_b32_e32 v2, v3
	v_add3_u32 v4, 0, v4, v41
	ds_read_b128 v[46:49], v4 offset:63744
	v_add3_u32 v4, 0, v44, v41
	ds_read_b128 v[50:53], v4 offset:26624
	v_mov_b32_e32 v4, v3
	v_mov_b32_e32 v5, v3
	v_mul_f32_e32 v2, 0, v2
	s_waitcnt lgkmcnt(0)
	s_nop 0
	v_mfma_f32_16x16x32_bf16 v[46:49], v[46:49], v[50:53], v[2:5]
	s_nop 2
	v_add3_u32 v2, s57, v44, v38
	s_nop 3
	v_cvt_pk_bf16_f32 v4, v46, v47
	v_cvt_pk_bf16_f32 v5, v48, v49
	ds_write_b64 v2, v[4:5] offset:29184

; __device__ __forceinline__ unsigned cvt_pk_bf16(float lo, float hi) { const f32x2 v = {lo, hi}; const bf16x2_t b = __builtin_convertvector(v, bf16x2_t); return __builtin_bit_cast(unsigned, b); }
; #define ZERO4() ((f32x4){opaque0(), 0.f, 0.f, 0.f} * 0.f)
; __device__ __forceinline__ void rwkv_state_phase(LAS unsigned char* lds, const unsigned char* img, bf16_t* y_, const RwScan& a_, const int vcu, const int G, const int tid0_) {
;     ...
;             if (wave < 4) {
;                 const int mt = wave >> 1, nt = wave & 1;
;                 f32x4 y = ZERO4();
; #pragma unroll
;                 for (int ks = 0; ks < 2; ++ks) y = __builtin_amdgcn_mfma_f32_16x16x32_bf16(ldfrag(S0, P64, 16 * mt + fr, 32 * ks + 8 * fq), ldfrag(RT, P64, 16 * nt + fr, 32 * ks + 8 * fq), y, 0, 0, 0);
;                 y = __builtin_amdgcn_mfma_f32_16x16x32_bf16(ldfrag(Ui, P32, 16 * mt + fr, 8 * fq), ldfrag(MbrT, P32, 16 * nt + fr, 8 * fq), y, 0, 0, 0);
;                 y = __builtin_amdgcn_mfma_f32_16x16x32_bf16(ldfrag(Vi, P32, 16 * mt + fr, 8 * fq), ldfrag(MkrT, P32, 16 * nt + fr, 8 * fq), y, 0, 0, 0);
;                 u32x2 o; o.x = cvt_pk_bf16(y[0], y[1]); o.y = cvt_pk_bf16(y[2], y[3]);
;                 *(u32x2*)(y_ + (size_t)(b * SEQ + t0 + 16 * nt + fr) * 1024 + h * 64 + half * 32 + 16 * mt + 4 * fq) = o;
;             }
.LBB0_853:
	s_and_b64 vcc, exec, s[8:9]
	s_waitcnt lgkmcnt(0)
	s_barrier
	s_cbranch_vccnz .LBB0_855
	v_mul_u32_u24_e32 v44, s67, v43
	v_mov_b32_e32 v2, v3
	v_add3_u32 v56, 0, v44, v41
	ds_read_b128 v[44:47], v56 offset:51456
	ds_read_b128 v[48:51], v42 offset:46848
	v_mul_f32_e32 v2, 0, v2
	v_mov_b32_e32 v4, v3
	v_mov_b32_e32 v5, v3
	v_readlane_b32 s9, v253, 58
	s_or_b32 s8, s54, s63
	s_waitcnt lgkmcnt(0)
	v_mfma_f32_16x16x32_bf16 v[44:47], v[44:47], v[48:51], v[2:5]
	ds_read_b128 v[48:51], v56 offset:51520
	ds_read_b128 v[52:55], v42 offset:46912
	s_nop 0
	v_lshlrev_b32_e32 v2, 6, v43
	v_sub_u32_e32 v2, v56, v2
	s_waitcnt lgkmcnt(0)
	v_mfma_f32_16x16x32_bf16 v[44:47], v[48:51], v[52:55], v[44:47]
	ds_read_b128 v[48:51], v2 offset:29184
	v_lshlrev_b32_e32 v2, 6, v40
	v_sub_u32_e32 v2, v42, v2
	ds_read_b128 v[52:55], v2 offset:58624
	v_mul_u32_u24_e32 v4, s66, v43
	v_add3_u32 v4, s9, v4, v41
	s_waitcnt lgkmcnt(0)
	v_mfma_f32_16x16x32_bf16 v[44:47], v[48:51], v[52:55], v[44:47]
	ds_read_b128 v[40:43], v4
	ds_read_b128 v[48:51], v2 offset:61184
	v_or_b32_e32 v2, s8, v39
	v_mov_b32_e32 v39, v3
	s_waitcnt lgkmcnt(0)
	v_mfma_f32_16x16x32_bf16 v[40:43], v[40:43], v[48:51], v[44:47]
	s_nop 7
	v_cvt_pk_bf16_f32 v4, v40, v41
	v_or_b32_e32 v40, 0x7e0, v2
	v_ashrrev_i32_e32 v41, 31, v40
	v_lshlrev_b64 v[40:41], 11, v[40:41]
	v_lshl_add_u64 v[40:41], s[2:3], 0, v[40:41]
	v_cvt_pk_bf16_f32 v5, v42, v43
	v_lshl_add_u64 v[38:39], v[40:41], 0, v[38:39]
	global_store_dwordx2 v[38:39], v[4:5], off
